# rwkv_chunk S4: the other 8 wave-wide sums via row_bcast DPP hoisted in front of the saveexec block (bit-identical)
# speedup vs baseline: 1.0021x; 1.0021x over previous
; __device__ __forceinline__ float bf2f(unsigned v) { return __uint_as_float(v << 16); }
; __device__ __forceinline__ void lds_st_bf16(LAS unsigned char* base, int idx, float v) { *(LAS bf16_t*)(base + idx * 2) = (bf16_t)f2bf(v); }
; __device__ __forceinline__ float wave_sum(float v) {
;     v = row16_sum(v);
;     const int iv = __float_as_int(v);
;     return (__int_as_float(__builtin_amdgcn_readlane(iv, 0)) + __int_as_float(__builtin_amdgcn_readlane(iv, 16))) + (__int_as_float(__builtin_amdgcn_readlane(iv, 32)) + __int_as_float(__builtin_amdgcn_readlane(iv, 48)));
; }
; __device__ __forceinline__ void phase_rwkv_chunk(const Ctx& c, const Args& a, int layer, const bf16_t* proj, const bf16_t* wlb, const bf16_t* alb, bf16_t* rwu, float* bonusg) {
;     ...
;             for (int w2 = 0; w2 < 8; ++w2) { const float v = sBS[w2 * 64 + j]; tot += v; off += (w2 < wave) ? v : 0.f; }
;             if (wave == 0) sWC[j] = __expf(tot);
;             float eWprev = __expf(off); const float eTot = __expf(tot); float tA[8], tV[8], tB[8], tK[8];
; #pragma unroll
;             for (int i = 0; i < 8; ++i) { const int tt = wave * 8 + i, t = t0 + tt;
;                 const float Lc = lcs[i] + off, al = als[i];
;                 const float rc = bf2f(rraw[i + 1]), kc = bf2f(kraw[i + 1]), vc = bf2f(vraw[i + 1]);
;                 const float r = rc + (bf2f(rraw[i]) - rc) * mur, k = kc + (bf2f(kraw[i]) - kc) * muk, v = vc + (bf2f(vraw[i]) - vc) * muv;
;                 float kk = k * kkw; const float n2 = wave_sum(kk * kk); kk = kk * rsqrtf(fmaxf(n2, 1e-24f));
;                 const float kp = k * (1.0f + (al - 1.0f) * kaw), av = -kk, bv = kk * al;
;                 const float eW = __expf(Lc), eInv = __builtin_amdgcn_rcpf(eW), eC = eTot * eInv; const float eWex = eWprev; eWprev = eW;
;                 lds_st_bf16(L + RC_AT, tt * 72 + j, av * eWex); tA[i] = av * eWex;
;                 lds_st_bf16(L + RC_RT, tt * 72 + j, r * eW); lds_st_bf16(L + RC_BT, tt * 72 + j, bv * eInv); lds_st_bf16(L + RC_KT, tt * 72 + j, kp * eInv);
;                 tV[i] = v; tB[i] = bv * eC; tK[i] = kp * eC;
;                 const float bon = wave_sum(r * kp * rk); if (lane == 0) bonusg[(size_t)t * 8 + h] = bon; }
.LBB0_699:
	v_readlane_b32 s14, v254, 45
	v_readlane_b32 s15, v254, 46
	s_lshl_b32 s29, s52, 3
	v_lshlrev_b32_e32 v10, 16, v37
	v_cndmask_b32_e64 v4, 0, v4, s[14:15]
	v_readlane_b32 s14, v254, 47
	v_readlane_b32 s15, v254, 48
	s_andn2_b32 s29, s29, 63
	v_add_f32_e32 v10, v171, v10
	v_cndmask_b32_e64 v11, 0, v11, s[14:15]
	v_readlane_b32 s14, v254, 49
	v_readlane_b32 s15, v254, 50
	v_add_f32_e32 v4, v4, v11
	v_mul_f32_e32 v10, 0xbfb8aa3b, v10
	v_cndmask_b32_e64 v8, 0, v8, s[14:15]
	v_readlane_b32 s14, v254, 51
	v_readlane_b32 s15, v254, 52
	v_add_f32_e32 v4, v4, v8
	v_cndmask_b32_e64 v8, 0, v9, s[38:39]
	v_cndmask_b32_e64 v6, 0, v6, s[14:15]
	v_readlane_b32 s14, v254, 53
	v_add_f32_e32 v4, v4, v8
	v_readlane_b32 s15, v254, 54
	v_add_f32_e32 v4, v4, v6
	v_exp_f32_e32 v10, v10
	v_cndmask_b32_e64 v6, 0, v7, s[14:15]
	v_readlane_b32 s14, v254, 55
	v_readlane_b32 s15, v254, 56
	v_add_f32_e32 v4, v4, v6
	v_lshlrev_b32_e32 v7, 16, v47
	v_cndmask_b32_e64 v2, 0, v2, s[14:15]
	v_readlane_b32 s14, v254, 57
	v_readlane_b32 s15, v254, 58
	v_add_f32_e32 v2, v4, v2
	v_sub_f32_e32 v0, 0, v0
	v_cndmask_b32_e64 v3, 0, v3, s[14:15]
	v_add_f32_e32 v22, v2, v3
	v_mul_f32_e32 v2, 0x3fb8aa3b, v22
	v_exp_f32_e32 v8, v2
	v_lshlrev_b32_e32 v2, 16, v50
	v_sub_f32_e32 v2, v2, v7
	v_fma_f32 v4, v2, v176, v7
	v_mul_f32_e32 v11, v4, v172
	v_mul_f32_e32 v2, v11, v11
	v_mov_b32_e32 v3, v1
	s_lshl_b32 s14, s20, 2
	v_readlane_b32 s15, v252, 23
	v_mov_b32_dpp v3, v2 quad_perm:[1,0,3,2] row_mask:0xf bank_mask:0xf
	v_fmac_f32_e32 v3, v11, v11
	s_add_u32 s22, s15, s14
	v_readlane_b32 s14, v252, 24
	v_add_f32_dpp v2, v3, v3 quad_perm:[2,3,0,1] row_mask:0xf bank_mask:0xf bound_ctrl:1
	s_addc_u32 s28, s14, 0
	v_add_f32_e32 v0, v0, v22
	v_add_f32_dpp v2, v2, v2 row_half_mirror row_mask:0xf bank_mask:0xf bound_ctrl:1
	v_mul_f32_e32 v0, 0x3fb8aa3b, v0
	v_exp_f32_e32 v9, v0
	v_add_f32_dpp v2, v2, v2 row_mirror row_mask:0xf bank_mask:0xf bound_ctrl:1
	v_add_f32_e32 v10, 1.0, v10
	s_nop 1
	v_add_f32_dpp v2, v2, v2 row_bcast:15 row_mask:0xa bank_mask:0xf
	s_nop 1
	v_add_f32_dpp v2, v2, v2 row_bcast:31 row_mask:0xc bank_mask:0xf
	s_nop 1
	v_readlane_b32 s20, v2, 63
	s_nop 1
	v_rcp_f32_e32 v18, v10
	v_mov_b32_e32 v2, s20
	v_max_f32_e32 v2, 0x179abe15, v2
	v_rsq_f32_e32 v2, v2
	v_lshlrev_b32_e32 v6, 16, v53
	v_lshlrev_b32_e32 v10, 16, v46
	v_sub_f32_e32 v0, v10, v6
	v_fma_f32 v20, v0, v175, v6
	v_mul_f32_e32 v0, v11, v2
	v_rcp_f32_e32 v11, v9
	v_add_f32_e32 v2, -1.0, v18
	v_fma_f32 v10, v173, v2, 1.0
	v_mul_f32_e32 v18, v18, v0
	v_mul_f32_e64 v0, v8, -v0
	v_pk_mul_f32 v[2:3], v[4:5], v[10:11]
	v_cvt_pk_bf16_f32 v4, v0, s0
	ds_write_b16 v127, v4 offset:52992
	v_mul_f32_e32 v4, v20, v9
	v_cvt_pk_bf16_f32 v4, v4, s0
	v_add_u32_e32 v8, 0x11700, v127
	ds_write_b16 v8, v4
	v_mul_f32_e32 v4, v11, v18
	v_cvt_pk_bf16_f32 v4, v4, s0
	v_add_u32_e32 v8, 0x13b00, v127
	ds_write_b16 v8, v4
	v_mul_f32_e32 v4, v2, v11
	v_cvt_pk_bf16_f32 v4, v4, s0
	v_add_u32_e32 v8, 0x15f00, v127
	ds_write_b16 v8, v4
	v_mul_f32_e32 v4, v20, v2
	v_mul_f32_e32 v8, v174, v4
	v_mov_b32_e32 v10, v1
	s_nop 1
	v_mov_b32_dpp v10, v8 quad_perm:[1,0,3,2] row_mask:0xf bank_mask:0xf
	v_fmac_f32_e32 v10, v174, v4
	s_nop 1
	v_add_f32_dpp v4, v10, v10 quad_perm:[2,3,0,1] row_mask:0xf bank_mask:0xf bound_ctrl:1
	s_nop 1
	v_add_f32_dpp v4, v4, v4 row_half_mirror row_mask:0xf bank_mask:0xf bound_ctrl:1
	s_nop 1
	v_add_f32_dpp v4, v4, v4 row_mirror row_mask:0xf bank_mask:0xf bound_ctrl:1
	s_nop 0
	s_nop 1
	v_add_f32_dpp v4, v4, v4 row_bcast:15 row_mask:0xa bank_mask:0xf
	s_nop 1
	v_add_f32_dpp v4, v4, v4 row_bcast:31 row_mask:0xc bank_mask:0xf
	s_nop 1
	v_readlane_b32 s20, v4, 63
	s_and_saveexec_b64 s[14:15], s[36:37]
	s_cbranch_execz .LBB0_701
	s_add_i32 s56, s29, s62
	s_ashr_i32 s57, s56, 31
	s_lshl_b64 s[56:57], s[56:57], 5
	s_add_u32 s56, s22, s56
	s_addc_u32 s57, s28, s57
	v_mov_b32_e32 v4, s20
	global_store_dword v1, v4, s[56:57]
.LBB0_701:
	s_or_b64 exec, exec, s[14:15]
	v_lshlrev_b32_e32 v4, 16, v39
	v_add_f32_e32 v4, v171, v4
	v_mul_f32_e32 v4, 0xbfb8aa3b, v4
	v_exp_f32_e32 v4, v4
	v_add_f32_e32 v20, v17, v22
	v_lshlrev_b32_e32 v17, 16, v59
	v_mov_b32_e32 v11, v1
	v_add_f32_e32 v4, 1.0, v4
	v_rcp_f32_e32 v21, v4
	v_sub_f32_e32 v4, v7, v17
	v_fma_f32 v4, v4, v176, v17
	v_mul_f32_e32 v7, v4, v172
	v_mul_f32_e32 v10, v7, v7
	v_lshlrev_b32_e32 v8, 16, v58
	v_sub_f32_e32 v6, v6, v8
	v_mov_b32_dpp v11, v10 quad_perm:[1,0,3,2] row_mask:0xf bank_mask:0xf
	v_fmac_f32_e32 v11, v7, v7
	v_fma_f32 v23, v6, v175, v8
	v_add_f32_e32 v6, -1.0, v21
	v_add_f32_dpp v10, v11, v11 quad_perm:[2,3,0,1] row_mask:0xf bank_mask:0xf bound_ctrl:1
	v_fma_f32 v24, v173, v6, 1.0
	s_nop 0
	v_add_f32_dpp v10, v10, v10 row_half_mirror row_mask:0xf bank_mask:0xf bound_ctrl:1
	s_nop 1
	v_add_f32_dpp v10, v10, v10 row_mirror row_mask:0xf bank_mask:0xf bound_ctrl:1
	s_nop 0
	s_nop 1
	v_add_f32_dpp v10, v10, v10 row_bcast:15 row_mask:0xa bank_mask:0xf
	s_nop 1
	v_add_f32_dpp v10, v10, v10 row_bcast:31 row_mask:0xc bank_mask:0xf
	s_nop 1
	v_readlane_b32 s20, v10, 63
	s_nop 1
	s_nop 0
	v_mov_b32_e32 v10, s20
	v_mul_f32_e32 v11, 0x3fb8aa3b, v20
	v_exp_f32_e32 v11, v11
	v_max_f32_e32 v10, 0x179abe15, v10
	v_rsq_f32_e32 v10, v10
	v_rcp_f32_e32 v25, v11
	v_mul_f32_e32 v10, v7, v10
	v_mul_f32_e64 v20, v9, -v10
	v_pk_mul_f32 v[6:7], v[4:5], v[24:25]
	v_cvt_pk_bf16_f32 v4, v20, s0
	ds_write_b16 v128, v4 offset:52992
	v_mul_f32_e32 v4, v23, v11
	v_mul_f32_e32 v21, v21, v10
	v_cvt_pk_bf16_f32 v4, v4, s0
	v_add_u32_e32 v9, 0x11700, v128
	ds_write_b16 v9, v4
	v_mul_f32_e32 v4, v25, v21
	v_cvt_pk_bf16_f32 v4, v4, s0
	v_add_u32_e32 v9, 0x13b00, v128
	ds_write_b16 v9, v4
	v_mul_f32_e32 v4, v6, v25
	v_cvt_pk_bf16_f32 v4, v4, s0
	v_add_u32_e32 v9, 0x15f00, v128
	ds_write_b16 v9, v4
	v_mul_f32_e32 v4, v23, v6
	v_mul_f32_e32 v9, v174, v4
	v_mov_b32_e32 v10, v1
	s_nop 1
	v_mov_b32_dpp v10, v9 quad_perm:[1,0,3,2] row_mask:0xf bank_mask:0xf
	v_fmac_f32_e32 v10, v174, v4
	s_nop 1
	v_add_f32_dpp v4, v10, v10 quad_perm:[2,3,0,1] row_mask:0xf bank_mask:0xf bound_ctrl:1
	s_nop 1
	v_add_f32_dpp v4, v4, v4 row_half_mirror row_mask:0xf bank_mask:0xf bound_ctrl:1
	s_nop 1
	v_add_f32_dpp v4, v4, v4 row_mirror row_mask:0xf bank_mask:0xf bound_ctrl:1
	s_nop 0
	s_nop 1
	v_add_f32_dpp v4, v4, v4 row_bcast:15 row_mask:0xa bank_mask:0xf
	s_nop 1
	v_add_f32_dpp v4, v4, v4 row_bcast:31 row_mask:0xc bank_mask:0xf
	s_nop 1
	v_readlane_b32 s20, v4, 63
	s_and_saveexec_b64 s[14:15], s[36:37]
	s_cbranch_execz .LBB0_703
	v_readlane_b32 s56, v254, 59
	s_add_i32 s56, s29, s56
	s_ashr_i32 s57, s56, 31
	s_lshl_b64 s[56:57], s[56:57], 5
	s_add_u32 s56, s22, s56
	s_addc_u32 s57, s28, s57
	v_mov_b32_e32 v4, s20
	global_store_dword v1, v4, s[56:57]
; __device__ __forceinline__ float bf2f(unsigned v) { return __uint_as_float(v << 16); }
; __device__ __forceinline__ void lds_st_bf16(LAS unsigned char* base, int idx, float v) { *(LAS bf16_t*)(base + idx * 2) = (bf16_t)f2bf(v); }
; __device__ __forceinline__ float wave_sum(float v) {
;     v = row16_sum(v);
;     const int iv = __float_as_int(v);
;     return (__int_as_float(__builtin_amdgcn_readlane(iv, 0)) + __int_as_float(__builtin_amdgcn_readlane(iv, 16))) + (__int_as_float(__builtin_amdgcn_readlane(iv, 32)) + __int_as_float(__builtin_amdgcn_readlane(iv, 48)));
; }
; __device__ __forceinline__ void phase_rwkv_chunk(const Ctx& c, const Args& a, int layer, const bf16_t* proj, const bf16_t* wlb, const bf16_t* alb, bf16_t* rwu, float* bonusg) {
;     ...
;             for (int i = 0; i < 8; ++i) { const int tt = wave * 8 + i, t = t0 + tt;
;                 const float Lc = lcs[i] + off, al = als[i];
;                 const float rc = bf2f(rraw[i + 1]), kc = bf2f(kraw[i + 1]), vc = bf2f(vraw[i + 1]);
;                 const float r = rc + (bf2f(rraw[i]) - rc) * mur, k = kc + (bf2f(kraw[i]) - kc) * muk, v = vc + (bf2f(vraw[i]) - vc) * muv;
;                 float kk = k * kkw; const float n2 = wave_sum(kk * kk); kk = kk * rsqrtf(fmaxf(n2, 1e-24f));
;                 const float kp = k * (1.0f + (al - 1.0f) * kaw), av = -kk, bv = kk * al;
;                 const float eW = __expf(Lc), eInv = __builtin_amdgcn_rcpf(eW), eC = eTot * eInv; const float eWex = eWprev; eWprev = eW;
;                 lds_st_bf16(L + RC_AT, tt * 72 + j, av * eWex); tA[i] = av * eWex;
;                 lds_st_bf16(L + RC_RT, tt * 72 + j, r * eW); lds_st_bf16(L + RC_BT, tt * 72 + j, bv * eInv); lds_st_bf16(L + RC_KT, tt * 72 + j, kp * eInv);
;                 tV[i] = v; tB[i] = bv * eC; tK[i] = kp * eC;
;                 const float bon = wave_sum(r * kp * rk); if (lane == 0) bonusg[(size_t)t * 8 + h] = bon; }
.LBB0_703:
	s_or_b64 exec, exec, s[14:15]
	v_lshlrev_b32_e32 v4, 16, v41
	v_add_f32_e32 v4, v171, v4
	v_mul_f32_e32 v4, 0xbfb8aa3b, v4
	v_exp_f32_e32 v4, v4
	v_lshlrev_b32_e32 v25, 16, v57
	v_add_f32_e32 v9, v15, v22
	v_mov_b32_e32 v24, v1
	v_add_f32_e32 v4, 1.0, v4
	v_rcp_f32_e32 v23, v4
	v_sub_f32_e32 v4, v17, v25
	v_fma_f32 v4, v4, v176, v25
	v_mul_f32_e32 v17, v4, v172
	v_mul_f32_e32 v15, v17, v17
	v_mul_f32_e32 v9, 0x3fb8aa3b, v9
	v_lshlrev_b32_e32 v10, 16, v62
	v_mov_b32_dpp v24, v15 quad_perm:[1,0,3,2] row_mask:0xf bank_mask:0xf
	v_fmac_f32_e32 v24, v17, v17
	v_sub_f32_e32 v8, v8, v10
	v_fma_f32 v28, v8, v175, v10
	v_add_f32_dpp v15, v24, v24 quad_perm:[2,3,0,1] row_mask:0xf bank_mask:0xf bound_ctrl:1
	v_add_f32_e32 v8, -1.0, v23
	s_nop 0
	v_add_f32_dpp v15, v15, v15 row_half_mirror row_mask:0xf bank_mask:0xf bound_ctrl:1
	s_nop 1
	v_add_f32_dpp v15, v15, v15 row_mirror row_mask:0xf bank_mask:0xf bound_ctrl:1
	s_nop 0
	v_mov_b32_e32 v26, v15
	s_nop 1
	v_add_f32_dpp v26, v26, v26 row_bcast:15 row_mask:0xa bank_mask:0xf
	s_nop 1
	v_add_f32_dpp v26, v26, v26 row_bcast:31 row_mask:0xc bank_mask:0xf
	s_nop 1
	v_readlane_b32 s20, v26, 63
	s_nop 1
	s_nop 0
	v_mov_b32_e32 v15, s20
	v_max_f32_e32 v15, 0x179abe15, v15
	v_rsq_f32_e32 v24, v15
	v_exp_f32_e32 v15, v9
	v_fma_f32 v26, v173, v8, 1.0
	v_mul_f32_e32 v17, v17, v24
	v_rcp_f32_e32 v27, v15
	v_mul_f32_e32 v24, v23, v17
	v_mul_f32_e64 v23, v11, -v17
	v_add_u32_e32 v11, 0x11700, v129
	v_pk_mul_f32 v[8:9], v[4:5], v[26:27]
	v_cvt_pk_bf16_f32 v4, v23, s0
	ds_write_b16 v129, v4 offset:52992
	v_mul_f32_e32 v4, v28, v15
	v_cvt_pk_bf16_f32 v4, v4, s0
	ds_write_b16 v11, v4
	v_mul_f32_e32 v4, v27, v24
	v_cvt_pk_bf16_f32 v4, v4, s0
	v_add_u32_e32 v11, 0x13b00, v129
	ds_write_b16 v11, v4
	v_mul_f32_e32 v4, v8, v27
	v_cvt_pk_bf16_f32 v4, v4, s0
	v_add_u32_e32 v11, 0x15f00, v129
	ds_write_b16 v11, v4
	v_mul_f32_e32 v4, v28, v8
	v_mul_f32_e32 v11, v174, v4
	v_mov_b32_e32 v17, v1
	s_nop 1
	v_mov_b32_dpp v17, v11 quad_perm:[1,0,3,2] row_mask:0xf bank_mask:0xf
	v_fmac_f32_e32 v17, v174, v4
	s_nop 1
	v_add_f32_dpp v4, v17, v17 quad_perm:[2,3,0,1] row_mask:0xf bank_mask:0xf bound_ctrl:1
	s_nop 1
	v_add_f32_dpp v4, v4, v4 row_half_mirror row_mask:0xf bank_mask:0xf bound_ctrl:1
	s_nop 1
	v_add_f32_dpp v4, v4, v4 row_mirror row_mask:0xf bank_mask:0xf bound_ctrl:1
	s_nop 0
	s_nop 1
	v_add_f32_dpp v4, v4, v4 row_bcast:15 row_mask:0xa bank_mask:0xf
	s_nop 1
	v_add_f32_dpp v4, v4, v4 row_bcast:31 row_mask:0xc bank_mask:0xf
	s_nop 1
	v_readlane_b32 s20, v4, 63
	s_and_saveexec_b64 s[14:15], s[36:37]
	s_cbranch_execz .LBB0_705
	v_readlane_b32 s56, v254, 60
	s_add_i32 s56, s29, s56
	s_ashr_i32 s57, s56, 31
	s_lshl_b64 s[56:57], s[56:57], 5
	s_add_u32 s56, s22, s56
	s_addc_u32 s57, s28, s57
	v_mov_b32_e32 v4, s20
	global_store_dword v1, v4, s[56:57]
.LBB0_705:
	s_or_b64 exec, exec, s[14:15]
	v_lshlrev_b32_e32 v4, 16, v43
	v_add_f32_e32 v4, v171, v4
	v_mul_f32_e32 v4, 0xbfb8aa3b, v4
	v_exp_f32_e32 v4, v4
	v_lshlrev_b32_e32 v27, 16, v66
	v_mov_b32_e32 v28, v1
	v_add_f32_e32 v11, v12, v22
	v_add_f32_e32 v4, 1.0, v4
	v_rcp_f32_e32 v26, v4
	v_sub_f32_e32 v4, v25, v27
	v_fma_f32 v4, v4, v176, v27
	v_mul_f32_e32 v25, v4, v172
	v_mul_f32_e32 v17, v25, v25
	v_mul_f32_e32 v11, 0x3fb8aa3b, v11
	v_lshlrev_b32_e32 v12, 16, v64
	v_mov_b32_dpp v28, v17 quad_perm:[1,0,3,2] row_mask:0xf bank_mask:0xf
	v_fmac_f32_e32 v28, v25, v25
	v_sub_f32_e32 v10, v10, v12
	v_fma_f32 v34, v10, v175, v12
	v_add_f32_dpp v17, v28, v28 quad_perm:[2,3,0,1] row_mask:0xf bank_mask:0xf bound_ctrl:1
	v_add_f32_e32 v10, -1.0, v26
	s_nop 0
	v_add_f32_dpp v17, v17, v17 row_half_mirror row_mask:0xf bank_mask:0xf bound_ctrl:1
	s_nop 1
	v_add_f32_dpp v17, v17, v17 row_mirror row_mask:0xf bank_mask:0xf bound_ctrl:1
	s_nop 0
	v_mov_b32_e32 v28, v17
	s_nop 1
	v_add_f32_dpp v28, v28, v28 row_bcast:15 row_mask:0xa bank_mask:0xf
	s_nop 1
	v_add_f32_dpp v28, v28, v28 row_bcast:31 row_mask:0xc bank_mask:0xf
	s_nop 1
	v_readlane_b32 s20, v28, 63
	s_nop 1
	s_nop 0
	v_mov_b32_e32 v17, s20
	v_max_f32_e32 v17, 0x179abe15, v17
	v_rsq_f32_e32 v28, v17
	v_exp_f32_e32 v17, v11
	v_mul_f32_e32 v25, v25, v28
	v_rcp_f32_e32 v29, v17
	v_fma_f32 v28, v173, v10, 1.0
	v_mul_f32_e32 v26, v26, v25
	v_mul_f32_e64 v25, v15, -v25
	v_pk_mul_f32 v[10:11], v[4:5], v[28:29]
	v_cvt_pk_bf16_f32 v4, v25, s0
	ds_write_b16 v130, v4 offset:52992
	v_mul_f32_e32 v4, v34, v17
	v_cvt_pk_bf16_f32 v4, v4, s0
	v_add_u32_e32 v15, 0x11700, v130
	ds_write_b16 v15, v4
	v_mul_f32_e32 v4, v29, v26
	v_cvt_pk_bf16_f32 v4, v4, s0
	v_add_u32_e32 v15, 0x13b00, v130
	ds_write_b16 v15, v4
	v_mul_f32_e32 v4, v10, v29
	v_cvt_pk_bf16_f32 v4, v4, s0
	v_add_u32_e32 v15, 0x15f00, v130
	ds_write_b16 v15, v4
	v_mul_f32_e32 v4, v34, v10
	v_mul_f32_e32 v15, v174, v4
	v_mov_b32_e32 v28, v1
	s_nop 1
	v_mov_b32_dpp v28, v15 quad_perm:[1,0,3,2] row_mask:0xf bank_mask:0xf
	v_fmac_f32_e32 v28, v174, v4
	s_nop 1
	v_add_f32_dpp v4, v28, v28 quad_perm:[2,3,0,1] row_mask:0xf bank_mask:0xf bound_ctrl:1
	s_nop 1
	v_add_f32_dpp v4, v4, v4 row_half_mirror row_mask:0xf bank_mask:0xf bound_ctrl:1
	s_nop 1
	v_add_f32_dpp v4, v4, v4 row_mirror row_mask:0xf bank_mask:0xf bound_ctrl:1
	s_nop 0
	s_nop 1
	v_add_f32_dpp v4, v4, v4 row_bcast:15 row_mask:0xa bank_mask:0xf
	s_nop 1
	v_add_f32_dpp v4, v4, v4 row_bcast:31 row_mask:0xc bank_mask:0xf
	s_nop 1
	v_readlane_b32 s20, v4, 63
	s_and_saveexec_b64 s[14:15], s[36:37]
	s_cbranch_execz .LBB0_707
	v_readlane_b32 s56, v254, 61
	s_add_i32 s56, s29, s56
	s_ashr_i32 s57, s56, 31
	s_lshl_b64 s[56:57], s[56:57], 5
	s_add_u32 s56, s22, s56
	s_addc_u32 s57, s28, s57
	v_mov_b32_e32 v4, s20
	global_store_dword v1, v4, s[56:57]
; __device__ __forceinline__ float bf2f(unsigned v) { return __uint_as_float(v << 16); }
; __device__ __forceinline__ void lds_st_bf16(LAS unsigned char* base, int idx, float v) { *(LAS bf16_t*)(base + idx * 2) = (bf16_t)f2bf(v); }
; __device__ __forceinline__ float wave_sum(float v) {
;     v = row16_sum(v);
;     const int iv = __float_as_int(v);
;     return (__int_as_float(__builtin_amdgcn_readlane(iv, 0)) + __int_as_float(__builtin_amdgcn_readlane(iv, 16))) + (__int_as_float(__builtin_amdgcn_readlane(iv, 32)) + __int_as_float(__builtin_amdgcn_readlane(iv, 48)));
; }
; __device__ __forceinline__ void phase_rwkv_chunk(const Ctx& c, const Args& a, int layer, const bf16_t* proj, const bf16_t* wlb, const bf16_t* alb, bf16_t* rwu, float* bonusg) {
;     ...
;             for (int i = 0; i < 8; ++i) { const int tt = wave * 8 + i, t = t0 + tt;
;                 const float Lc = lcs[i] + off, al = als[i];
;                 const float rc = bf2f(rraw[i + 1]), kc = bf2f(kraw[i + 1]), vc = bf2f(vraw[i + 1]);
;                 const float r = rc + (bf2f(rraw[i]) - rc) * mur, k = kc + (bf2f(kraw[i]) - kc) * muk, v = vc + (bf2f(vraw[i]) - vc) * muv;
;                 float kk = k * kkw; const float n2 = wave_sum(kk * kk); kk = kk * rsqrtf(fmaxf(n2, 1e-24f));
;                 const float kp = k * (1.0f + (al - 1.0f) * kaw), av = -kk, bv = kk * al;
;                 const float eW = __expf(Lc), eInv = __builtin_amdgcn_rcpf(eW), eC = eTot * eInv; const float eWex = eWprev; eWprev = eW;
;                 lds_st_bf16(L + RC_AT, tt * 72 + j, av * eWex); tA[i] = av * eWex;
;                 lds_st_bf16(L + RC_RT, tt * 72 + j, r * eW); lds_st_bf16(L + RC_BT, tt * 72 + j, bv * eInv); lds_st_bf16(L + RC_KT, tt * 72 + j, kp * eInv);
;                 tV[i] = v; tB[i] = bv * eC; tK[i] = kp * eC;
;                 const float bon = wave_sum(r * kp * rk); if (lane == 0) bonusg[(size_t)t * 8 + h] = bon; }
.LBB0_707:
	s_or_b64 exec, exec, s[14:15]
	v_lshlrev_b32_e32 v4, 16, v45
	v_add_f32_e32 v4, v171, v4
	v_mul_f32_e32 v4, 0xbfb8aa3b, v4
	v_exp_f32_e32 v4, v4
	v_lshlrev_b32_e32 v34, 16, v65
	v_mov_b32_e32 v29, v1
	v_add_f32_e32 v13, v13, v22
	v_add_f32_e32 v4, 1.0, v4
	v_rcp_f32_e32 v35, v4
	v_sub_f32_e32 v4, v27, v34
	v_fma_f32 v4, v4, v176, v34
	v_mul_f32_e32 v27, v4, v172
	v_mul_f32_e32 v28, v27, v27
	v_mul_f32_e32 v13, 0x3fb8aa3b, v13
	v_lshlrev_b32_e32 v15, 16, v68
	v_mov_b32_dpp v29, v28 quad_perm:[1,0,3,2] row_mask:0xf bank_mask:0xf
	v_fmac_f32_e32 v29, v27, v27
	v_sub_f32_e32 v12, v12, v15
	v_fma_f32 v180, v12, v175, v15
	v_add_f32_dpp v28, v29, v29 quad_perm:[2,3,0,1] row_mask:0xf bank_mask:0xf bound_ctrl:1
	v_add_f32_e32 v12, -1.0, v35
	v_fma_f32 v178, v173, v12, 1.0
	v_add_f32_dpp v28, v28, v28 row_half_mirror row_mask:0xf bank_mask:0xf bound_ctrl:1
	s_nop 1
	v_add_f32_dpp v28, v28, v28 row_mirror row_mask:0xf bank_mask:0xf bound_ctrl:1
	s_nop 0
	s_nop 1
	v_add_f32_dpp v28, v28, v28 row_bcast:15 row_mask:0xa bank_mask:0xf
	s_nop 1
	v_add_f32_dpp v28, v28, v28 row_bcast:31 row_mask:0xc bank_mask:0xf
	s_nop 1
	v_readlane_b32 s20, v28, 63
	s_nop 1
	s_nop 0
	v_mov_b32_e32 v28, s20
	v_exp_f32_e32 v29, v13
	v_max_f32_e32 v28, 0x179abe15, v28
	v_rsq_f32_e32 v28, v28
	v_rcp_f32_e32 v179, v29
	v_mul_f32_e32 v27, v27, v28
	v_mul_f32_e32 v28, v35, v27
	v_mul_f32_e64 v27, v17, -v27
	v_pk_mul_f32 v[12:13], v[4:5], v[178:179]
	v_cvt_pk_bf16_f32 v4, v27, s0
	ds_write_b16 v131, v4 offset:52992
	v_mul_f32_e32 v4, v180, v29
	v_cvt_pk_bf16_f32 v4, v4, s0
	v_add_u32_e32 v17, 0x11700, v131
	ds_write_b16 v17, v4
	v_mul_f32_e32 v4, v179, v28
	v_cvt_pk_bf16_f32 v4, v4, s0
	v_add_u32_e32 v17, 0x13b00, v131
	ds_write_b16 v17, v4
	v_mul_f32_e32 v4, v12, v179
	v_cvt_pk_bf16_f32 v4, v4, s0
	v_add_u32_e32 v17, 0x15f00, v131
	ds_write_b16 v17, v4
	v_mul_f32_e32 v4, v180, v12
	v_mul_f32_e32 v17, v174, v4
	v_mov_b32_e32 v35, v1
	s_nop 1
	v_mov_b32_dpp v35, v17 quad_perm:[1,0,3,2] row_mask:0xf bank_mask:0xf
	v_fmac_f32_e32 v35, v174, v4
	s_nop 1
	v_add_f32_dpp v4, v35, v35 quad_perm:[2,3,0,1] row_mask:0xf bank_mask:0xf bound_ctrl:1
	s_nop 1
	v_add_f32_dpp v4, v4, v4 row_half_mirror row_mask:0xf bank_mask:0xf bound_ctrl:1
	s_nop 1
	v_add_f32_dpp v4, v4, v4 row_mirror row_mask:0xf bank_mask:0xf bound_ctrl:1
	s_nop 0
	s_nop 1
	v_add_f32_dpp v4, v4, v4 row_bcast:15 row_mask:0xa bank_mask:0xf
	s_nop 1
	v_add_f32_dpp v4, v4, v4 row_bcast:31 row_mask:0xc bank_mask:0xf
	s_nop 1
	v_readlane_b32 s20, v4, 63
	s_and_saveexec_b64 s[14:15], s[36:37]
	s_cbranch_execz .LBB0_709
	v_readlane_b32 s56, v254, 62
	s_add_i32 s56, s29, s56
	s_ashr_i32 s57, s56, 31
	s_lshl_b64 s[56:57], s[56:57], 5
	s_add_u32 s56, s22, s56
	s_addc_u32 s57, s28, s57
	v_mov_b32_e32 v4, s20
	global_store_dword v1, v4, s[56:57]
.LBB0_709:
	s_or_b64 exec, exec, s[14:15]
	v_lshlrev_b32_e32 v4, 16, v51
	v_add_f32_e32 v4, v171, v4
	v_mul_f32_e32 v4, 0xbfb8aa3b, v4
	v_exp_f32_e32 v4, v4
	v_lshlrev_b32_e32 v178, 16, v72
	v_mov_b32_e32 v35, v1
	v_add_f32_e32 v14, v22, v14
	v_add_f32_e32 v4, 1.0, v4
	v_rcp_f32_e32 v179, v4
	v_sub_f32_e32 v4, v34, v178
	v_fma_f32 v4, v4, v176, v178
	v_mul_f32_e32 v180, v4, v172
	v_mul_f32_e32 v34, v180, v180
	v_mul_f32_e32 v14, 0x3fb8aa3b, v14
	v_lshlrev_b32_e32 v17, 16, v70
	v_mov_b32_dpp v35, v34 quad_perm:[1,0,3,2] row_mask:0xf bank_mask:0xf
	v_fmac_f32_e32 v35, v180, v180
	s_nop 1
	v_add_f32_dpp v34, v35, v35 quad_perm:[2,3,0,1] row_mask:0xf bank_mask:0xf bound_ctrl:1
	s_nop 1
	v_add_f32_dpp v34, v34, v34 row_half_mirror row_mask:0xf bank_mask:0xf bound_ctrl:1
	s_nop 1
	v_add_f32_dpp v34, v34, v34 row_mirror row_mask:0xf bank_mask:0xf bound_ctrl:1
	s_nop 0
	s_nop 1
	v_add_f32_dpp v34, v34, v34 row_bcast:15 row_mask:0xa bank_mask:0xf
	s_nop 1
	v_add_f32_dpp v34, v34, v34 row_bcast:31 row_mask:0xc bank_mask:0xf
	s_nop 1
	v_readlane_b32 s20, v34, 63
	s_nop 1
	s_nop 0
	v_mov_b32_e32 v34, s20
	v_exp_f32_e32 v35, v14
	v_max_f32_e32 v34, 0x179abe15, v34
	v_rsq_f32_e32 v34, v34
	v_sub_f32_e32 v14, v15, v17
	v_rcp_f32_e32 v181, v35
	v_fma_f32 v182, v14, v175, v17
	v_mul_f32_e32 v183, v180, v34
	v_add_f32_e32 v14, -1.0, v179
	v_fma_f32 v180, v173, v14, 1.0
	v_mul_f32_e64 v29, v29, -v183
	v_pk_mul_f32 v[14:15], v[4:5], v[180:181]
	v_cvt_pk_bf16_f32 v4, v29, s0
	ds_write_b16 v132, v4 offset:52992
	v_mul_f32_e32 v4, v182, v35
	v_mul_f32_e32 v34, v179, v183
	v_cvt_pk_bf16_f32 v4, v4, s0
	v_add_u32_e32 v179, 0x11700, v132
	ds_write_b16 v179, v4
	v_mul_f32_e32 v4, v181, v34
	v_cvt_pk_bf16_f32 v4, v4, s0
	v_add_u32_e32 v179, 0x13b00, v132
	ds_write_b16 v179, v4
	v_mul_f32_e32 v4, v14, v181
	v_cvt_pk_bf16_f32 v4, v4, s0
	v_add_u32_e32 v179, 0x15f00, v132
	ds_write_b16 v179, v4
	v_mul_f32_e32 v4, v182, v14
	v_mul_f32_e32 v179, v174, v4
	v_mov_b32_e32 v180, v1
	s_nop 1
	v_mov_b32_dpp v180, v179 quad_perm:[1,0,3,2] row_mask:0xf bank_mask:0xf
	v_fmac_f32_e32 v180, v174, v4
	s_nop 1
	v_add_f32_dpp v4, v180, v180 quad_perm:[2,3,0,1] row_mask:0xf bank_mask:0xf bound_ctrl:1
	s_nop 1
	v_add_f32_dpp v4, v4, v4 row_half_mirror row_mask:0xf bank_mask:0xf bound_ctrl:1
	s_nop 1
	v_add_f32_dpp v4, v4, v4 row_mirror row_mask:0xf bank_mask:0xf bound_ctrl:1
	s_nop 0
	s_nop 1
	v_add_f32_dpp v4, v4, v4 row_bcast:15 row_mask:0xa bank_mask:0xf
	s_nop 1
	v_add_f32_dpp v4, v4, v4 row_bcast:31 row_mask:0xc bank_mask:0xf
	s_nop 1
	v_readlane_b32 s20, v4, 63
	s_and_saveexec_b64 s[14:15], s[36:37]
	s_cbranch_execz .LBB0_711
	v_readlane_b32 s56, v254, 63
	s_add_i32 s56, s29, s56
	s_ashr_i32 s57, s56, 31
	s_lshl_b64 s[56:57], s[56:57], 5
	s_add_u32 s56, s22, s56
	s_addc_u32 s57, s28, s57
	v_mov_b32_e32 v4, s20
	global_store_dword v1, v4, s[56:57]
; __device__ __forceinline__ float bf2f(unsigned v) { return __uint_as_float(v << 16); }
; __device__ __forceinline__ void lds_st_bf16(LAS unsigned char* base, int idx, float v) { *(LAS bf16_t*)(base + idx * 2) = (bf16_t)f2bf(v); }
; __device__ __forceinline__ float wave_sum(float v) {
;     v = row16_sum(v);
;     const int iv = __float_as_int(v);
;     return (__int_as_float(__builtin_amdgcn_readlane(iv, 0)) + __int_as_float(__builtin_amdgcn_readlane(iv, 16))) + (__int_as_float(__builtin_amdgcn_readlane(iv, 32)) + __int_as_float(__builtin_amdgcn_readlane(iv, 48)));
; }
; __device__ __forceinline__ void phase_rwkv_chunk(const Ctx& c, const Args& a, int layer, const bf16_t* proj, const bf16_t* wlb, const bf16_t* alb, bf16_t* rwu, float* bonusg) {
;     ...
;             for (int i = 0; i < 8; ++i) { const int tt = wave * 8 + i, t = t0 + tt;
;                 const float Lc = lcs[i] + off, al = als[i];
;                 const float rc = bf2f(rraw[i + 1]), kc = bf2f(kraw[i + 1]), vc = bf2f(vraw[i + 1]);
;                 const float r = rc + (bf2f(rraw[i]) - rc) * mur, k = kc + (bf2f(kraw[i]) - kc) * muk, v = vc + (bf2f(vraw[i]) - vc) * muv;
;                 float kk = k * kkw; const float n2 = wave_sum(kk * kk); kk = kk * rsqrtf(fmaxf(n2, 1e-24f));
;                 const float kp = k * (1.0f + (al - 1.0f) * kaw), av = -kk, bv = kk * al;
;                 const float eW = __expf(Lc), eInv = __builtin_amdgcn_rcpf(eW), eC = eTot * eInv; const float eWex = eWprev; eWprev = eW;
;                 lds_st_bf16(L + RC_AT, tt * 72 + j, av * eWex); tA[i] = av * eWex;
;                 lds_st_bf16(L + RC_RT, tt * 72 + j, r * eW); lds_st_bf16(L + RC_BT, tt * 72 + j, bv * eInv); lds_st_bf16(L + RC_KT, tt * 72 + j, kp * eInv);
;                 tV[i] = v; tB[i] = bv * eC; tK[i] = kp * eC;
;                 const float bon = wave_sum(r * kp * rk); if (lane == 0) bonusg[(size_t)t * 8 + h] = bon; }
.LBB0_711:
	s_or_b64 exec, exec, s[14:15]
	v_lshlrev_b32_e32 v4, 16, v54
	v_add_f32_e32 v4, v171, v4
	v_mul_f32_e32 v4, 0xbfb8aa3b, v4
	v_exp_f32_e32 v4, v4
	v_lshlrev_b32_e32 v180, 16, v71
	v_mov_b32_e32 v179, v1
	v_add_f32_e32 v16, v22, v16
	v_add_f32_e32 v4, 1.0, v4
	v_rcp_f32_e32 v184, v4
	v_sub_f32_e32 v4, v178, v180
	v_fma_f32 v4, v4, v176, v180
	v_mul_f32_e32 v182, v4, v172
	v_mul_f32_e32 v178, v182, v182
	v_mul_f32_e32 v16, 0x3fb8aa3b, v16
	v_lshlrev_b32_e32 v181, 16, v77
	v_mov_b32_dpp v179, v178 quad_perm:[1,0,3,2] row_mask:0xf bank_mask:0xf
	v_fmac_f32_e32 v179, v182, v182
	s_nop 1
	v_add_f32_dpp v178, v179, v179 quad_perm:[2,3,0,1] row_mask:0xf bank_mask:0xf bound_ctrl:1
	s_nop 1
	v_add_f32_dpp v178, v178, v178 row_half_mirror row_mask:0xf bank_mask:0xf bound_ctrl:1
	s_nop 1
	v_add_f32_dpp v178, v178, v178 row_mirror row_mask:0xf bank_mask:0xf bound_ctrl:1
	s_nop 0
	s_nop 1
	v_add_f32_dpp v178, v178, v178 row_bcast:15 row_mask:0xa bank_mask:0xf
	s_nop 1
	v_add_f32_dpp v178, v178, v178 row_bcast:31 row_mask:0xc bank_mask:0xf
	s_nop 1
	v_readlane_b32 s20, v178, 63
	s_nop 1
	s_nop 0
	v_mov_b32_e32 v178, s20
	v_exp_f32_e32 v179, v16
	v_max_f32_e32 v178, 0x179abe15, v178
	v_rsq_f32_e32 v178, v178
	v_sub_f32_e32 v16, v17, v181
	v_rcp_f32_e32 v183, v179
	v_fma_f32 v185, v16, v175, v181
	v_mul_f32_e32 v187, v182, v178
	v_add_f32_e32 v16, -1.0, v184
	v_fma_f32 v182, v173, v16, 1.0
	v_mul_f32_e64 v35, v35, -v187
	v_pk_mul_f32 v[16:17], v[4:5], v[182:183]
	v_cvt_pk_bf16_f32 v4, v35, s0
	ds_write_b16 v133, v4 offset:52992
	v_mul_f32_e32 v4, v185, v179
	v_mul_f32_e32 v178, v184, v187
	v_cvt_pk_bf16_f32 v4, v4, s0
	v_add_u32_e32 v182, 0x11700, v133
	ds_write_b16 v182, v4
	v_mul_f32_e32 v4, v183, v178
	v_cvt_pk_bf16_f32 v4, v4, s0
	v_add_u32_e32 v182, 0x13b00, v133
	ds_write_b16 v182, v4
	v_mul_f32_e32 v4, v16, v183
	v_cvt_pk_bf16_f32 v4, v4, s0
	v_add_u32_e32 v182, 0x15f00, v133
	ds_write_b16 v182, v4
	v_mul_f32_e32 v4, v185, v16
	v_mul_f32_e32 v182, v174, v4
	v_mov_b32_e32 v183, v1
	s_nop 1
	v_mov_b32_dpp v183, v182 quad_perm:[1,0,3,2] row_mask:0xf bank_mask:0xf
	v_fmac_f32_e32 v183, v174, v4
	s_nop 1
	v_add_f32_dpp v4, v183, v183 quad_perm:[2,3,0,1] row_mask:0xf bank_mask:0xf bound_ctrl:1
	s_nop 1
	v_add_f32_dpp v4, v4, v4 row_half_mirror row_mask:0xf bank_mask:0xf bound_ctrl:1
	s_nop 1
	v_add_f32_dpp v4, v4, v4 row_mirror row_mask:0xf bank_mask:0xf bound_ctrl:1
	s_nop 0
	s_nop 1
	v_add_f32_dpp v4, v4, v4 row_bcast:15 row_mask:0xa bank_mask:0xf
	s_nop 1
	v_add_f32_dpp v4, v4, v4 row_bcast:31 row_mask:0xc bank_mask:0xf
	s_nop 1
	v_readlane_b32 s20, v4, 63
	s_and_saveexec_b64 s[14:15], s[36:37]
	s_cbranch_execz .LBB0_713
	v_readlane_b32 s56, v255, 0
	s_add_i32 s56, s29, s56
	s_ashr_i32 s57, s56, 31
	s_lshl_b64 s[56:57], s[56:57], 5
	s_add_u32 s56, s22, s56
	s_addc_u32 s57, s28, s57
	v_mov_b32_e32 v4, s20
	global_store_dword v1, v4, s[56:57]
.LBB0_713:
	s_or_b64 exec, exec, s[14:15]
	v_lshlrev_b32_e32 v4, 16, v61
	v_add_f32_e32 v4, v171, v4
	v_mul_f32_e32 v4, 0xbfb8aa3b, v4
	v_exp_f32_e32 v4, v4
	v_lshlrev_b32_e32 v183, 16, v80
	v_add_f32_e32 v19, v22, v19
	v_sub_f32_e32 v22, v181, v183
	v_add_f32_e32 v4, 1.0, v4
	v_rcp_f32_e32 v182, v4
	v_lshlrev_b32_e32 v4, 16, v81
	v_fmac_f32_e32 v183, v22, v175
	v_sub_f32_e32 v22, v180, v4
	v_fmac_f32_e32 v4, v22, v176
	v_mul_f32_e32 v22, v4, v172
	v_mul_f32_e32 v180, v22, v22
	v_mov_b32_e32 v181, v1
	v_mul_f32_e32 v19, 0x3fb8aa3b, v19
	s_nop 0
	v_mov_b32_dpp v181, v180 quad_perm:[1,0,3,2] row_mask:0xf bank_mask:0xf
	v_fmac_f32_e32 v181, v22, v22
	s_nop 1
	v_add_f32_dpp v180, v181, v181 quad_perm:[2,3,0,1] row_mask:0xf bank_mask:0xf bound_ctrl:1
	s_nop 1
	v_add_f32_dpp v180, v180, v180 row_half_mirror row_mask:0xf bank_mask:0xf bound_ctrl:1
	s_nop 1
	v_add_f32_dpp v180, v180, v180 row_mirror row_mask:0xf bank_mask:0xf bound_ctrl:1
	s_nop 0
	s_nop 1
	v_add_f32_dpp v180, v180, v180 row_bcast:15 row_mask:0xa bank_mask:0xf
	s_nop 1
	v_add_f32_dpp v180, v180, v180 row_bcast:31 row_mask:0xc bank_mask:0xf
	s_nop 1
	v_readlane_b32 s20, v180, 63
	s_nop 1
	s_nop 0
	v_mov_b32_e32 v180, s20
	v_max_f32_e32 v180, 0x179abe15, v180
	v_rsq_f32_e32 v180, v180
	s_nop 0
	v_mul_f32_e32 v184, v22, v180
	v_add_f32_e32 v22, -1.0, v182
	v_fma_f32 v180, v173, v22, 1.0
	v_mul_f32_e32 v22, v182, v184
	v_exp_f32_e32 v182, v19
	v_mul_f32_e64 v19, v179, -v184
	v_cvt_pk_bf16_f32 v179, v19, s0
	ds_write_b16 v134, v179 offset:52992
	v_rcp_f32_e32 v181, v182
	v_mul_f32_e32 v179, v183, v182
	v_cvt_pk_bf16_f32 v179, v179, s0
	v_pk_mul_f32 v[4:5], v[4:5], v[180:181]
	v_add_u32_e32 v180, 0x11700, v134
	ds_write_b16 v180, v179
	v_mul_f32_e32 v179, v181, v22
	v_cvt_pk_bf16_f32 v179, v179, s0
	v_add_u32_e32 v180, 0x13b00, v134
	ds_write_b16 v180, v179
	v_mul_f32_e32 v179, v4, v181
	v_cvt_pk_bf16_f32 v179, v179, s0
	v_add_u32_e32 v180, 0x15f00, v134
	ds_write_b16 v180, v179
	v_mul_f32_e32 v179, v183, v4
	v_mul_f32_e32 v180, v174, v179
	v_mov_b32_e32 v181, v1
	s_nop 1
	v_mov_b32_dpp v181, v180 quad_perm:[1,0,3,2] row_mask:0xf bank_mask:0xf
	v_fmac_f32_e32 v181, v174, v179
	s_nop 1
	v_add_f32_dpp v179, v181, v181 quad_perm:[2,3,0,1] row_mask:0xf bank_mask:0xf bound_ctrl:1
	s_nop 1
	v_add_f32_dpp v179, v179, v179 row_half_mirror row_mask:0xf bank_mask:0xf bound_ctrl:1
	s_nop 1
	v_add_f32_dpp v179, v179, v179 row_mirror row_mask:0xf bank_mask:0xf bound_ctrl:1
	s_nop 0
	s_nop 1
	v_add_f32_dpp v179, v179, v179 row_bcast:15 row_mask:0xa bank_mask:0xf
	s_nop 1
	v_add_f32_dpp v179, v179, v179 row_bcast:31 row_mask:0xc bank_mask:0xf
	s_nop 1
	v_readlane_b32 s20, v179, 63
	s_and_saveexec_b64 s[14:15], s[36:37]
	s_cbranch_execz .LBB0_715
	v_readlane_b32 s56, v255, 1
	s_add_i32 s56, s29, s56
	s_ashr_i32 s57, s56, 31
	s_lshl_b64 s[56:57], s[56:57], 5
	s_add_u32 s56, s22, s56
	s_addc_u32 s57, s28, s57
	v_mov_b32_e32 v179, s20
	global_store_dword v1, v179, s[56:57]
